# GEMM unit start: 128 accumulator zeroing v_mov_b32 -> 64 v_mov_b64 (all four GEMM phases)
# speedup vs baseline: 1.0044x; 1.0044x over previous
; template <class Epi, class Sched>
; __device__ __forceinline__ void gemm_phase(LAS unsigned char* lds, const bf16_t* Abase, const int K, const Sched& S, const Epi& E, const int wvid) {
;     ...
; #pragma unroll
;         for (int a = 0; a < 2; ++a)
; #pragma unroll
;             for (int b = 0; b < 2; ++b)
; #pragma unroll
;                 for (int m = 0; m < 4; ++m)
; #pragma unroll
;                     for (int n = 0; n < 2; ++n) acc[a][b][m][n] = (f32x4){0.f, 0.f, 0.f, 0.f};
;         cur = nxt; cB = nB; ++ui;
.LBB0_124:
	s_ashr_i32 s25, s24, 31
	s_lshl_b64 s[26:27], s[24:25], 19
	s_add_u32 s26, s38, s26
	s_addc_u32 s27, s39, s27
	s_and_b64 s[28:29], s[0:1], exec
	s_cselect_b32 s25, s27, s5
	s_cselect_b32 s58, s26, s4
	s_add_u32 s59, s4, 0x100
	v_mov_b32_e32 v2, 0
	s_addc_u32 s60, s5, 0
	s_mov_b32 s61, -2
	s_mov_b64 s[4:5], 0
	v_mov_b32_e32 v3, v2
	v_mov_b64_e32 v[4:5], 0
	v_mov_b64_e32 v[6:7], 0
	v_mov_b64_e32 v[8:9], 0
	v_mov_b64_e32 v[18:19], 0
	v_mov_b64_e32 v[20:21], 0
	v_mov_b64_e32 v[22:23], 0
	v_mov_b64_e32 v[24:25], 0
	v_mov_b64_e32 v[34:35], 0
	v_mov_b64_e32 v[36:37], 0
	v_mov_b64_e32 v[38:39], 0
	v_mov_b64_e32 v[40:41], 0
	v_mov_b64_e32 v[50:51], 0
	v_mov_b64_e32 v[52:53], 0
	v_mov_b64_e32 v[54:55], 0
	v_mov_b64_e32 v[56:57], 0
	v_mov_b64_e32 v[10:11], 0
	v_mov_b64_e32 v[12:13], 0
	v_mov_b64_e32 v[14:15], 0
	v_mov_b64_e32 v[16:17], 0
	v_mov_b64_e32 v[26:27], 0
	v_mov_b64_e32 v[28:29], 0
	v_mov_b64_e32 v[30:31], 0
	v_mov_b64_e32 v[32:33], 0
	v_mov_b64_e32 v[42:43], 0
	v_mov_b64_e32 v[44:45], 0
	v_mov_b64_e32 v[46:47], 0
	v_mov_b64_e32 v[48:49], 0
	v_mov_b64_e32 v[58:59], 0
	v_mov_b64_e32 v[60:61], 0
	v_mov_b64_e32 v[62:63], 0
	v_mov_b64_e32 v[64:65], 0
	v_mov_b64_e32 v[66:67], 0
	v_mov_b64_e32 v[68:69], 0
	v_mov_b64_e32 v[70:71], 0
	v_mov_b64_e32 v[72:73], 0
	v_mov_b64_e32 v[74:75], 0
	v_mov_b64_e32 v[76:77], 0
	v_mov_b64_e32 v[78:79], 0
	v_mov_b64_e32 v[80:81], 0
	v_mov_b64_e32 v[90:91], 0
	v_mov_b64_e32 v[92:93], 0
	v_mov_b64_e32 v[94:95], 0
	v_mov_b64_e32 v[96:97], 0
	v_mov_b64_e32 v[106:107], 0
	v_mov_b64_e32 v[108:109], 0
	v_mov_b64_e32 v[110:111], 0
	v_mov_b64_e32 v[112:113], 0
	v_mov_b64_e32 v[82:83], 0
	v_mov_b64_e32 v[84:85], 0
	v_mov_b64_e32 v[86:87], 0
	v_mov_b64_e32 v[88:89], 0
	v_mov_b64_e32 v[98:99], 0
	v_mov_b64_e32 v[100:101], 0
	v_mov_b64_e32 v[102:103], 0
	v_mov_b64_e32 v[104:105], 0
	v_mov_b64_e32 v[114:115], 0
	v_mov_b64_e32 v[116:117], 0
	v_mov_b64_e32 v[118:119], 0
	v_mov_b64_e32 v[120:121], 0
	v_mov_b64_e32 v[122:123], 0
	v_mov_b64_e32 v[124:125], 0
	v_mov_b64_e32 v[126:127], 0
	v_mov_b64_e32 v[128:129], 0

; template <class Epi, class Sched>
; __device__ __forceinline__ void gemm_phase(LAS unsigned char* lds, const bf16_t* Abase, const int K, const Sched& S, const Epi& E, const int wvid) {
;     ...
; #pragma unroll
;         for (int a = 0; a < 2; ++a)
; #pragma unroll
;             for (int b = 0; b < 2; ++b)
; #pragma unroll
;                 for (int m = 0; m < 4; ++m)
; #pragma unroll
;                     for (int n = 0; n < 2; ++n) acc[a][b][m][n] = (f32x4){0.f, 0.f, 0.f, 0.f};
;         cur = nxt; cB = nB; ++ui;
.LBB0_1001:
	s_ashr_i32 s11, s10, 31
	s_ashr_i32 s17, s16, 31
	s_xor_b64 s[20:21], s[24:25], -1
	s_lshl_b64 s[18:19], s[10:11], 19
	s_lshl_b64 s[28:29], s[16:17], 1
	s_add_u32 s11, s38, s18
	s_addc_u32 s17, s39, s19
	s_add_u32 s18, s11, s28
	s_addc_u32 s19, s17, s29
	s_and_b64 s[28:29], s[24:25], exec
	s_cselect_b32 s11, s19, s27
	s_cselect_b32 s17, s18, s26
	s_add_u32 s23, s26, 0x100
	v_mov_b32_e32 v2, 0
	s_addc_u32 s58, s27, 0
	s_add_i32 s59, s57, -2
	s_mov_b32 s60, 0
	s_mov_b64 s[26:27], 0
	v_mov_b32_e32 v3, v2
	v_mov_b64_e32 v[4:5], 0
	v_mov_b64_e32 v[6:7], 0
	v_mov_b64_e32 v[8:9], 0
	v_mov_b64_e32 v[10:11], 0
	v_mov_b64_e32 v[12:13], 0
	v_mov_b64_e32 v[14:15], 0
	v_mov_b64_e32 v[16:17], 0
	v_mov_b64_e32 v[22:23], 0
	v_mov_b64_e32 v[24:25], 0
	v_mov_b64_e32 v[30:31], 0
	v_mov_b64_e32 v[32:33], 0
	v_mov_b64_e32 v[38:39], 0
	v_mov_b64_e32 v[40:41], 0
	v_mov_b64_e32 v[46:47], 0
	v_mov_b64_e32 v[48:49], 0
	v_mov_b64_e32 v[18:19], 0
	v_mov_b64_e32 v[20:21], 0
	v_mov_b64_e32 v[26:27], 0
	v_mov_b64_e32 v[28:29], 0
	v_mov_b64_e32 v[34:35], 0
	v_mov_b64_e32 v[36:37], 0
	v_mov_b64_e32 v[42:43], 0
	v_mov_b64_e32 v[44:45], 0
	v_mov_b64_e32 v[50:51], 0
	v_mov_b64_e32 v[52:53], 0
	v_mov_b64_e32 v[54:55], 0
	v_mov_b64_e32 v[56:57], 0
	v_mov_b64_e32 v[58:59], 0
	v_mov_b64_e32 v[60:61], 0
	v_mov_b64_e32 v[62:63], 0
	v_mov_b64_e32 v[64:65], 0
	v_mov_b64_e32 v[66:67], 0
	s_waitcnt vmcnt(0)
	v_mov_b64_e32 v[68:69], 0
	v_mov_b64_e32 v[70:71], 0
	v_mov_b64_e32 v[72:73], 0
	v_mov_b64_e32 v[74:75], 0
	v_mov_b64_e32 v[76:77], 0
	v_mov_b64_e32 v[78:79], 0
	v_mov_b64_e32 v[80:81], 0
	v_mov_b64_e32 v[82:83], 0
	v_mov_b64_e32 v[84:85], 0
	v_mov_b64_e32 v[86:87], 0
	v_mov_b64_e32 v[88:89], 0
	v_mov_b64_e32 v[90:91], 0
	v_mov_b64_e32 v[92:93], 0
	v_mov_b64_e32 v[94:95], 0
	v_mov_b64_e32 v[96:97], 0
	v_mov_b64_e32 v[98:99], 0
	v_mov_b64_e32 v[100:101], 0
	v_mov_b64_e32 v[102:103], 0
	v_mov_b64_e32 v[104:105], 0
	v_mov_b64_e32 v[106:107], 0
	v_mov_b64_e32 v[108:109], 0
	v_mov_b64_e32 v[110:111], 0
	v_mov_b64_e32 v[112:113], 0
	v_mov_b64_e32 v[114:115], 0
	v_mov_b64_e32 v[116:117], 0
	v_mov_b64_e32 v[118:119], 0
	v_mov_b64_e32 v[120:121], 0
	v_mov_b64_e32 v[122:123], 0
	v_mov_b64_e32 v[124:125], 0
	v_mov_b64_e32 v[126:127], 0
	v_mov_b64_e32 v[128:129], 0

;     __device__ __forceinline__ const char* b_ptr(const Unit& u) const { return (const char*)Bt + ((size_t)u.pn * BM * K + u.koff) * 2; }
;     __device__ __forceinline__ const char* b_ptr(const Unit& u) const { return (const char*)Bt + ((size_t)u.e * bstride + (size_t)u.pn * BM * K) * 2; }
; template <class Epi, class Sched>
; __device__ __forceinline__ void gemm_phase(LAS unsigned char* lds, const bf16_t* Abase, const int K, const Sched& S, const Epi& E, const int wvid) {
;     ...
; #pragma unroll
;         for (int a = 0; a < 2; ++a)
; #pragma unroll
;             for (int b = 0; b < 2; ++b)
; #pragma unroll
;                 for (int m = 0; m < 4; ++m)
; #pragma unroll
;                     for (int n = 0; n < 2; ++n) acc[a][b][m][n] = (f32x4){0.f, 0.f, 0.f, 0.f};
;         cur = nxt; cB = nB; ++ui;
.LBB0_1208:
	s_ashr_i32 s23, s22, 31
	s_lshl_b64 s[4:5], s[22:23], 19
	v_ashrrev_i32_e32 v191, 31, v190
	s_add_u32 s4, s36, s4
	v_lshlrev_b64 v[4:5], 21, v[190:191]
	s_addc_u32 s5, s37, s5
	v_lshl_add_u64 v[194:195], s[4:5], 0, v[4:5]
	s_mov_b64 s[4:5], 0x100
	v_cndmask_b32_e64 v229, v2, v194, s[0:1]
	v_lshl_add_u64 v[196:197], v[2:3], 0, s[4:5]
	v_mov_b32_e32 v2, 0
	v_cndmask_b32_e64 v191, v3, v195, s[0:1]
	v_add_u32_e32 v230, -1, v193
	v_add_u32_e32 v231, 0x80, v227
	s_mov_b32 s23, -2
	s_mov_b64 s[26:27], 0
	v_mov_b32_e32 v3, v2
	v_mov_b64_e32 v[4:5], 0
	v_mov_b64_e32 v[6:7], 0
	v_mov_b64_e32 v[8:9], 0
	v_mov_b64_e32 v[18:19], 0
	v_mov_b64_e32 v[20:21], 0
	v_mov_b64_e32 v[22:23], 0
	v_mov_b64_e32 v[24:25], 0
	v_mov_b64_e32 v[34:35], 0
	v_mov_b64_e32 v[36:37], 0
	v_mov_b64_e32 v[38:39], 0
	v_mov_b64_e32 v[40:41], 0
	v_mov_b64_e32 v[50:51], 0
	v_mov_b64_e32 v[52:53], 0
	v_mov_b64_e32 v[54:55], 0
	v_mov_b64_e32 v[56:57], 0
	v_mov_b64_e32 v[10:11], 0
	v_mov_b64_e32 v[12:13], 0
	v_mov_b64_e32 v[14:15], 0
	v_mov_b64_e32 v[16:17], 0
	v_mov_b64_e32 v[26:27], 0
	v_mov_b64_e32 v[28:29], 0
	v_mov_b64_e32 v[30:31], 0
	v_mov_b64_e32 v[32:33], 0
	v_mov_b64_e32 v[42:43], 0
	v_mov_b64_e32 v[44:45], 0
	v_mov_b64_e32 v[46:47], 0
	v_mov_b64_e32 v[48:49], 0
	v_mov_b64_e32 v[58:59], 0
	v_mov_b64_e32 v[60:61], 0
	v_mov_b64_e32 v[62:63], 0
	v_mov_b64_e32 v[64:65], 0
	v_mov_b64_e32 v[66:67], 0
	v_mov_b64_e32 v[68:69], 0
	v_mov_b64_e32 v[70:71], 0
	v_mov_b64_e32 v[72:73], 0
	v_mov_b64_e32 v[74:75], 0
	v_mov_b64_e32 v[76:77], 0
	v_mov_b64_e32 v[78:79], 0
	v_mov_b64_e32 v[80:81], 0
	v_mov_b64_e32 v[82:83], 0
	v_mov_b64_e32 v[84:85], 0
	v_mov_b64_e32 v[86:87], 0
	v_mov_b64_e32 v[88:89], 0
	v_mov_b64_e32 v[98:99], 0
	v_mov_b64_e32 v[100:101], 0
	v_mov_b64_e32 v[102:103], 0
	v_mov_b64_e32 v[104:105], 0
	v_mov_b64_e32 v[90:91], 0
	v_mov_b64_e32 v[92:93], 0
	v_mov_b64_e32 v[94:95], 0
	v_mov_b64_e32 v[96:97], 0
	v_mov_b64_e32 v[106:107], 0
	v_mov_b64_e32 v[108:109], 0
	v_mov_b64_e32 v[110:111], 0
	v_mov_b64_e32 v[112:113], 0
	v_mov_b64_e32 v[114:115], 0
	v_mov_b64_e32 v[116:117], 0
	v_mov_b64_e32 v[118:119], 0
	v_mov_b64_e32 v[120:121], 0
	v_mov_b64_e32 v[122:123], 0
	v_mov_b64_e32 v[124:125], 0
	v_mov_b64_e32 v[126:127], 0
	v_mov_b64_e32 v[128:129], 0

;     __device__ __forceinline__ const char* b_ptr(const Unit& u) const { return (const char*)Bt + ((size_t)u.pn * BM * K + u.koff) * 2; }
;     __device__ __forceinline__ const char* b_ptr(const Unit& u) const { return (const char*)Bt + ((size_t)u.e * bstride + (size_t)u.pn * BM * K) * 2; }
; template <class Epi, class Sched>
; __device__ __forceinline__ void gemm_phase(LAS unsigned char* lds, const bf16_t* Abase, const int K, const Sched& S, const Epi& E, const int wvid) {
;     ...
; #pragma unroll
;         for (int a = 0; a < 2; ++a)
; #pragma unroll
;             for (int b = 0; b < 2; ++b)
; #pragma unroll
;                 for (int m = 0; m < 4; ++m)
; #pragma unroll
;                     for (int n = 0; n < 2; ++n) acc[a][b][m][n] = (f32x4){0.f, 0.f, 0.f, 0.f};
;         cur = nxt; cB = nB; ++ui;
.LBB0_1475:
	s_ashr_i32 s25, s24, 31
	s_lshl_b64 s[4:5], s[24:25], 18
	v_ashrrev_i32_e32 v191, 31, v190
	s_add_u32 s4, s36, s4
	v_lshlrev_b64 v[4:5], 20, v[190:191]
	s_addc_u32 s5, s37, s5
	v_lshl_add_u64 v[194:195], s[4:5], 0, v[4:5]
	s_mov_b64 s[4:5], 0x100
	v_cndmask_b32_e64 v229, v2, v194, s[0:1]
	v_lshl_add_u64 v[196:197], v[2:3], 0, s[4:5]
	v_mov_b32_e32 v2, 0
	v_cndmask_b32_e64 v191, v3, v195, s[0:1]
	v_add_u32_e32 v230, 0x80, v228
	s_mov_b32 s25, -2
	s_mov_b64 s[26:27], 0
	v_mov_b32_e32 v3, v2
	v_mov_b64_e32 v[4:5], 0
	v_mov_b64_e32 v[6:7], 0
	v_mov_b64_e32 v[8:9], 0
	v_mov_b64_e32 v[18:19], 0
	v_mov_b64_e32 v[20:21], 0
	v_mov_b64_e32 v[22:23], 0
	v_mov_b64_e32 v[24:25], 0
	v_mov_b64_e32 v[34:35], 0
	v_mov_b64_e32 v[36:37], 0
	v_mov_b64_e32 v[38:39], 0
	v_mov_b64_e32 v[40:41], 0
	v_mov_b64_e32 v[50:51], 0
	v_mov_b64_e32 v[52:53], 0
	v_mov_b64_e32 v[54:55], 0
	v_mov_b64_e32 v[56:57], 0
	v_mov_b64_e32 v[10:11], 0
	v_mov_b64_e32 v[12:13], 0
	v_mov_b64_e32 v[14:15], 0
	v_mov_b64_e32 v[16:17], 0
	v_mov_b64_e32 v[26:27], 0
	v_mov_b64_e32 v[28:29], 0
	v_mov_b64_e32 v[30:31], 0
	v_mov_b64_e32 v[32:33], 0
	v_mov_b64_e32 v[42:43], 0
	v_mov_b64_e32 v[44:45], 0
	v_mov_b64_e32 v[46:47], 0
	v_mov_b64_e32 v[48:49], 0
	v_mov_b64_e32 v[58:59], 0
	v_mov_b64_e32 v[60:61], 0
	v_mov_b64_e32 v[62:63], 0
	v_mov_b64_e32 v[64:65], 0
	v_mov_b64_e32 v[66:67], 0
	v_mov_b64_e32 v[68:69], 0
	v_mov_b64_e32 v[70:71], 0
	v_mov_b64_e32 v[72:73], 0
	v_mov_b64_e32 v[74:75], 0
	v_mov_b64_e32 v[76:77], 0
	v_mov_b64_e32 v[78:79], 0
	v_mov_b64_e32 v[80:81], 0
	v_mov_b64_e32 v[82:83], 0
	v_mov_b64_e32 v[84:85], 0
	v_mov_b64_e32 v[86:87], 0
	v_mov_b64_e32 v[88:89], 0
	v_mov_b64_e32 v[90:91], 0
	v_mov_b64_e32 v[92:93], 0
	v_mov_b64_e32 v[94:95], 0
	v_mov_b64_e32 v[96:97], 0
	v_mov_b64_e32 v[98:99], 0
	v_mov_b64_e32 v[100:101], 0
	v_mov_b64_e32 v[102:103], 0
	v_mov_b64_e32 v[104:105], 0
	v_mov_b64_e32 v[106:107], 0
	v_mov_b64_e32 v[108:109], 0
	v_mov_b64_e32 v[110:111], 0
	v_mov_b64_e32 v[112:113], 0
	v_mov_b64_e32 v[114:115], 0
	v_mov_b64_e32 v[116:117], 0
	v_mov_b64_e32 v[118:119], 0
	v_mov_b64_e32 v[120:121], 0
	v_mov_b64_e32 v[122:123], 0
	v_mov_b64_e32 v[124:125], 0
	v_mov_b64_e32 v[126:127], 0
	v_mov_b64_e32 v[128:129], 0
